# P1 rotary section: three blocks of cos/sin loads in flight per row half (rotating register sets, counted vmcnt waits) instead of load-wait per block
# baseline (speedup 1.0000x reference)
; #define LAS __attribute__((address_space(3)))
; #define EPI_BAR() do { asm volatile("s_waitcnt lgkmcnt(0)" ::: "memory"); __builtin_amdgcn_s_barrier(); asm volatile("" ::: "memory"); } while (0)
;     __device__ __forceinline__ void operator()(Acc& acc, const Unit& u, int wr, int wc, int fr, int fq, LAS unsigned char* le, int wid, int lane, int& cpm) const {
;     ...
;             EPI_BAR();
;             const float* gn = gains + ((type == 0) ? 0 : (type == 1) ? 128 : (type == 3) ? 256 : 384) + wc * 32 + fq * 8;
;             const f32x4 g0 = *(const f32x4*)gn, g1 = *(const f32x4*)(gn + 4);
; #pragma unroll
;             for (int ai = 0; ai < 2; ++ai)
; #pragma unroll
;                 for (int m = 0; m < 4; ++m)
; #pragma unroll
;                     for (int bj = 0; bj < 2; ++bj) {
;                         const f32x4 pp = *(const LAS f32x4*)(P + ((ai * 128 + wr * 64 + m * 16 + fr) * 2 + bj) * 4);
;                         const float rn = 1.0f / sqrtf(((pp[0] + pp[1]) + (pp[2] + pp[3])) * (1.0f / HD) + EPS);
;                         acc[ai][bj][m][0] = acc[ai][bj][m][0] * rn * g0; acc[ai][bj][m][1] = acc[ai][bj][m][1] * rn * g1;
;                     }
;             if (type >= 3 && wc == 0) {
.LBB0_306:
	s_or_b64 exec, exec, s[14:15]
	s_cmp_eq_u32 s3, 3
	s_movk_i32 s14, 0x180
	s_cselect_b32 s14, 0x100, s14
	s_cmp_lg_u32 s3, 1
	s_cselect_b32 s14, s14, 0x80
	s_cmp_gt_u32 s24, 3
	s_cselect_b32 s14, s14, 0
	s_lshl_b32 s16, s14, 2
	s_waitcnt lgkmcnt(0)
	s_barrier
	v_lshl_add_u64 v[132:133], v[162:163], 0, s[16:17]
	v_add_u32_e32 v140, s61, v199
	s_waitcnt lgkmcnt(0)
	global_load_dwordx4 v[128:131], v[132:133], off offset:16
	s_nop 0
	global_load_dwordx4 v[132:135], v[132:133], off
	ds_read_b128 v[136:139], v140
	ds_read_b128 v[140:143], v140 offset:16
	s_cmp_lt_i32 s3, 3
	s_waitcnt lgkmcnt(0)
	v_mov_b32_e32 v174, v137
	v_mov_b32_e32 v175, v138
	v_mov_b32_e32 v137, v139
	v_pk_add_f32 v[136:137], v[174:175], v[136:137]
	s_nop 0
	v_add_f32_e32 v136, v136, v137
	v_fmamk_f32 v136, v136, 0x3c000000, v205
	v_rsq_f32_e32 v136, v136
	s_nop 0
	v_pk_mul_f32 v[80:81], v[80:81], v[136:137] op_sel_hi:[1,0]
	v_pk_mul_f32 v[82:83], v[82:83], v[136:137] op_sel_hi:[1,0]
	v_pk_mul_f32 v[92:93], v[92:93], v[136:137] op_sel_hi:[1,0]
	v_pk_mul_f32 v[94:95], v[94:95], v[136:137] op_sel_hi:[1,0]
	v_mov_b32_e32 v136, v141
	v_mov_b32_e32 v137, v142
	v_mov_b32_e32 v141, v143
	v_pk_add_f32 v[136:137], v[136:137], v[140:141]
	s_waitcnt vmcnt(0)
	v_pk_mul_f32 v[94:95], v[130:131], v[94:95]
	v_add_f32_e32 v136, v136, v137
	v_fmamk_f32 v136, v136, 0x3c000000, v205
	v_pk_mul_f32 v[82:83], v[134:135], v[82:83]
	v_pk_mul_f32 v[80:81], v[132:133], v[80:81]
	v_pk_mul_f32 v[92:93], v[128:129], v[92:93]
	v_rsq_f32_e32 v136, v136
	s_nop 0
	v_add_u32_e32 v140, s63, v199
	v_pk_mul_f32 v[120:121], v[120:121], v[136:137] op_sel_hi:[1,0]
	v_pk_mul_f32 v[122:123], v[122:123], v[136:137] op_sel_hi:[1,0]
	v_pk_mul_f32 v[124:125], v[124:125], v[136:137] op_sel_hi:[1,0]
	v_pk_mul_f32 v[126:127], v[126:127], v[136:137] op_sel_hi:[1,0]
	ds_read_b128 v[136:139], v140
	ds_read_b128 v[140:143], v140 offset:16
	v_pk_mul_f32 v[122:123], v[134:135], v[122:123]
	v_pk_mul_f32 v[120:121], v[132:133], v[120:121]
	v_pk_mul_f32 v[126:127], v[130:131], v[126:127]
	s_waitcnt lgkmcnt(1)
	v_mov_b32_e32 v174, v137
	v_mov_b32_e32 v175, v138
	v_mov_b32_e32 v137, v139
	v_pk_add_f32 v[136:137], v[174:175], v[136:137]
	v_pk_mul_f32 v[124:125], v[128:129], v[124:125]
	v_add_f32_e32 v136, v136, v137
	v_fmamk_f32 v136, v136, 0x3c000000, v205
	v_rsq_f32_e32 v136, v136
	s_nop 0
	v_pk_mul_f32 v[52:53], v[52:53], v[136:137] op_sel_hi:[1,0]
	v_pk_mul_f32 v[54:55], v[54:55], v[136:137] op_sel_hi:[1,0]
	v_pk_mul_f32 v[68:69], v[68:69], v[136:137] op_sel_hi:[1,0]
	v_pk_mul_f32 v[70:71], v[70:71], v[136:137] op_sel_hi:[1,0]
	s_waitcnt lgkmcnt(0)
	v_mov_b32_e32 v136, v141
	v_mov_b32_e32 v137, v142
	v_mov_b32_e32 v141, v143
	v_pk_add_f32 v[136:137], v[136:137], v[140:141]
	v_pk_mul_f32 v[54:55], v[134:135], v[54:55]
	v_add_f32_e32 v136, v136, v137
	v_fmamk_f32 v136, v136, 0x3c000000, v205
	v_pk_mul_f32 v[52:53], v[132:133], v[52:53]
	v_pk_mul_f32 v[70:71], v[130:131], v[70:71]
	v_pk_mul_f32 v[68:69], v[128:129], v[68:69]
	v_rsq_f32_e32 v136, v136
	s_nop 0
	v_add_u32_e32 v140, s64, v199
	v_pk_mul_f32 v[104:105], v[104:105], v[136:137] op_sel_hi:[1,0]
	v_pk_mul_f32 v[106:107], v[106:107], v[136:137] op_sel_hi:[1,0]
	v_pk_mul_f32 v[112:113], v[112:113], v[136:137] op_sel_hi:[1,0]
	v_pk_mul_f32 v[114:115], v[114:115], v[136:137] op_sel_hi:[1,0]
	ds_read_b128 v[136:139], v140
	ds_read_b128 v[140:143], v140 offset:16
	v_pk_mul_f32 v[106:107], v[134:135], v[106:107]
	v_pk_mul_f32 v[104:105], v[132:133], v[104:105]
	v_pk_mul_f32 v[114:115], v[130:131], v[114:115]
	s_waitcnt lgkmcnt(1)
	v_mov_b32_e32 v174, v137
	v_mov_b32_e32 v175, v138
	v_mov_b32_e32 v137, v139
	v_pk_add_f32 v[136:137], v[174:175], v[136:137]
	v_pk_mul_f32 v[112:113], v[128:129], v[112:113]
	v_add_f32_e32 v136, v136, v137
	v_fmamk_f32 v136, v136, 0x3c000000, v205
	v_rsq_f32_e32 v136, v136
	s_nop 0
	v_pk_mul_f32 v[28:29], v[28:29], v[136:137] op_sel_hi:[1,0]
	v_pk_mul_f32 v[30:31], v[30:31], v[136:137] op_sel_hi:[1,0]
	v_pk_mul_f32 v[36:37], v[36:37], v[136:137] op_sel_hi:[1,0]
	v_pk_mul_f32 v[38:39], v[38:39], v[136:137] op_sel_hi:[1,0]
	s_waitcnt lgkmcnt(0)
	v_mov_b32_e32 v136, v141
	v_mov_b32_e32 v137, v142
	v_mov_b32_e32 v141, v143
	v_pk_add_f32 v[136:137], v[136:137], v[140:141]
	v_pk_mul_f32 v[30:31], v[134:135], v[30:31]
	v_add_f32_e32 v136, v136, v137
	v_fmamk_f32 v136, v136, 0x3c000000, v205
	v_pk_mul_f32 v[28:29], v[132:133], v[28:29]
	v_pk_mul_f32 v[38:39], v[130:131], v[38:39]
	v_pk_mul_f32 v[36:37], v[128:129], v[36:37]
	v_rsq_f32_e32 v136, v136
	s_nop 0
	v_add_u32_e32 v140, s65, v199
	v_pk_mul_f32 v[84:85], v[84:85], v[136:137] op_sel_hi:[1,0]
	v_pk_mul_f32 v[86:87], v[86:87], v[136:137] op_sel_hi:[1,0]
	v_pk_mul_f32 v[96:97], v[96:97], v[136:137] op_sel_hi:[1,0]
	v_pk_mul_f32 v[98:99], v[98:99], v[136:137] op_sel_hi:[1,0]
	ds_read_b128 v[136:139], v140
	ds_read_b128 v[140:143], v140 offset:16
	v_pk_mul_f32 v[86:87], v[134:135], v[86:87]
	v_pk_mul_f32 v[84:85], v[132:133], v[84:85]
	v_pk_mul_f32 v[98:99], v[130:131], v[98:99]
	s_waitcnt lgkmcnt(1)
	v_mov_b32_e32 v174, v137
	v_mov_b32_e32 v175, v138
	v_mov_b32_e32 v137, v139
	v_pk_add_f32 v[136:137], v[174:175], v[136:137]
	v_pk_mul_f32 v[96:97], v[128:129], v[96:97]
	v_add_f32_e32 v136, v136, v137
	v_fmamk_f32 v136, v136, 0x3c000000, v205
	v_rsq_f32_e32 v136, v136
	s_nop 0
	v_pk_mul_f32 v[8:9], v[8:9], v[136:137] op_sel_hi:[1,0]
	v_pk_mul_f32 v[10:11], v[10:11], v[136:137] op_sel_hi:[1,0]
	v_pk_mul_f32 v[16:17], v[16:17], v[136:137] op_sel_hi:[1,0]
	v_pk_mul_f32 v[18:19], v[18:19], v[136:137] op_sel_hi:[1,0]
	s_waitcnt lgkmcnt(0)
; #define LAS __attribute__((address_space(3)))
;     __device__ __forceinline__ void operator()(Acc& acc, const Unit& u, int wr, int wc, int fr, int fq, LAS unsigned char* le, int wid, int lane, int& cpm) const {
;     ...
; #pragma unroll
;             for (int ai = 0; ai < 2; ++ai)
; #pragma unroll
;                 for (int m = 0; m < 4; ++m)
; #pragma unroll
;                     for (int bj = 0; bj < 2; ++bj) {
;                         const f32x4 pp = *(const LAS f32x4*)(P + ((ai * 128 + wr * 64 + m * 16 + fr) * 2 + bj) * 4);
;                         const float rn = 1.0f / sqrtf(((pp[0] + pp[1]) + (pp[2] + pp[3])) * (1.0f / HD) + EPS);
;                         acc[ai][bj][m][0] = acc[ai][bj][m][0] * rn * g0; acc[ai][bj][m][1] = acc[ai][bj][m][1] * rn * g1;
;                     }
;             if (type >= 3 && wc == 0) {
	v_mov_b32_e32 v136, v141
	v_mov_b32_e32 v137, v142
	v_mov_b32_e32 v141, v143
	v_pk_add_f32 v[136:137], v[136:137], v[140:141]
	v_pk_mul_f32 v[10:11], v[134:135], v[10:11]
	v_add_f32_e32 v136, v136, v137
	v_fmamk_f32 v136, v136, 0x3c000000, v205
	v_pk_mul_f32 v[8:9], v[132:133], v[8:9]
	v_pk_mul_f32 v[18:19], v[130:131], v[18:19]
	v_pk_mul_f32 v[16:17], v[128:129], v[16:17]
	v_rsq_f32_e32 v136, v136
	s_nop 0
	v_add_u32_e32 v140, s66, v199
	v_pk_mul_f32 v[48:49], v[48:49], v[136:137] op_sel_hi:[1,0]
	v_pk_mul_f32 v[50:51], v[50:51], v[136:137] op_sel_hi:[1,0]
	v_pk_mul_f32 v[64:65], v[64:65], v[136:137] op_sel_hi:[1,0]
	v_pk_mul_f32 v[66:67], v[66:67], v[136:137] op_sel_hi:[1,0]
	ds_read_b128 v[136:139], v140
	ds_read_b128 v[140:143], v140 offset:16
	v_pk_mul_f32 v[50:51], v[134:135], v[50:51]
	v_pk_mul_f32 v[48:49], v[132:133], v[48:49]
	v_pk_mul_f32 v[66:67], v[130:131], v[66:67]
	s_waitcnt lgkmcnt(1)
	v_mov_b32_e32 v174, v137
	v_mov_b32_e32 v175, v138
	v_mov_b32_e32 v137, v139
	v_pk_add_f32 v[136:137], v[174:175], v[136:137]
	v_pk_mul_f32 v[64:65], v[128:129], v[64:65]
	v_add_f32_e32 v136, v136, v137
	v_fmamk_f32 v136, v136, 0x3c000000, v205
	v_rsq_f32_e32 v136, v136
	s_nop 0
	v_pk_mul_f32 v[56:57], v[56:57], v[136:137] op_sel_hi:[1,0]
	v_pk_mul_f32 v[58:59], v[58:59], v[136:137] op_sel_hi:[1,0]
	v_pk_mul_f32 v[72:73], v[72:73], v[136:137] op_sel_hi:[1,0]
	v_pk_mul_f32 v[74:75], v[74:75], v[136:137] op_sel_hi:[1,0]
	s_waitcnt lgkmcnt(0)
	v_mov_b32_e32 v136, v141
	v_mov_b32_e32 v137, v142
	v_mov_b32_e32 v141, v143
	v_pk_add_f32 v[136:137], v[136:137], v[140:141]
	v_pk_mul_f32 v[58:59], v[134:135], v[58:59]
	v_add_f32_e32 v136, v136, v137
	v_fmamk_f32 v136, v136, 0x3c000000, v205
	v_pk_mul_f32 v[56:57], v[132:133], v[56:57]
	v_pk_mul_f32 v[74:75], v[130:131], v[74:75]
	v_pk_mul_f32 v[72:73], v[128:129], v[72:73]
	v_rsq_f32_e32 v136, v136
	s_nop 0
	v_add_u32_e32 v140, s67, v199
	v_pk_mul_f32 v[108:109], v[108:109], v[136:137] op_sel_hi:[1,0]
	v_pk_mul_f32 v[110:111], v[110:111], v[136:137] op_sel_hi:[1,0]
	v_pk_mul_f32 v[116:117], v[116:117], v[136:137] op_sel_hi:[1,0]
	v_pk_mul_f32 v[118:119], v[118:119], v[136:137] op_sel_hi:[1,0]
	ds_read_b128 v[136:139], v140
	ds_read_b128 v[140:143], v140 offset:16
	v_pk_mul_f32 v[110:111], v[134:135], v[110:111]
	v_pk_mul_f32 v[108:109], v[132:133], v[108:109]
	v_pk_mul_f32 v[118:119], v[130:131], v[118:119]
	s_waitcnt lgkmcnt(1)
	v_mov_b32_e32 v174, v137
	v_mov_b32_e32 v175, v138
	v_mov_b32_e32 v137, v139
	v_pk_add_f32 v[136:137], v[174:175], v[136:137]
	v_pk_mul_f32 v[116:117], v[128:129], v[116:117]
	v_add_f32_e32 v136, v136, v137
	v_fmamk_f32 v136, v136, 0x3c000000, v205
	v_rsq_f32_e32 v136, v136
	s_nop 0
	v_pk_mul_f32 v[32:33], v[32:33], v[136:137] op_sel_hi:[1,0]
	v_pk_mul_f32 v[34:35], v[34:35], v[136:137] op_sel_hi:[1,0]
	v_pk_mul_f32 v[40:41], v[40:41], v[136:137] op_sel_hi:[1,0]
	v_pk_mul_f32 v[42:43], v[42:43], v[136:137] op_sel_hi:[1,0]
	s_waitcnt lgkmcnt(0)
	v_mov_b32_e32 v136, v141
	v_mov_b32_e32 v137, v142
	v_mov_b32_e32 v141, v143
	v_pk_add_f32 v[136:137], v[136:137], v[140:141]
	v_pk_mul_f32 v[34:35], v[134:135], v[34:35]
	v_add_f32_e32 v136, v136, v137
	v_fmamk_f32 v136, v136, 0x3c000000, v205
	v_pk_mul_f32 v[32:33], v[132:133], v[32:33]
	v_pk_mul_f32 v[42:43], v[130:131], v[42:43]
	v_pk_mul_f32 v[40:41], v[128:129], v[40:41]
	v_rsq_f32_e32 v136, v136
	s_nop 0
	v_add_u32_e32 v140, s68, v199
	v_pk_mul_f32 v[88:89], v[88:89], v[136:137] op_sel_hi:[1,0]
	v_pk_mul_f32 v[90:91], v[90:91], v[136:137] op_sel_hi:[1,0]
	v_pk_mul_f32 v[100:101], v[100:101], v[136:137] op_sel_hi:[1,0]
	v_pk_mul_f32 v[102:103], v[102:103], v[136:137] op_sel_hi:[1,0]
	ds_read_b128 v[136:139], v140
	ds_read_b128 v[140:143], v140 offset:16
	v_pk_mul_f32 v[90:91], v[134:135], v[90:91]
	v_pk_mul_f32 v[88:89], v[132:133], v[88:89]
	v_pk_mul_f32 v[102:103], v[130:131], v[102:103]
	s_waitcnt lgkmcnt(1)
	v_mov_b32_e32 v174, v137
	v_mov_b32_e32 v175, v138
	v_mov_b32_e32 v137, v139
	v_pk_add_f32 v[136:137], v[174:175], v[136:137]
	v_pk_mul_f32 v[100:101], v[128:129], v[100:101]
	v_add_f32_e32 v136, v136, v137
	v_fmamk_f32 v136, v136, 0x3c000000, v205
	v_rsq_f32_e32 v136, v136
	s_nop 0
	v_pk_mul_f32 v[12:13], v[12:13], v[136:137] op_sel_hi:[1,0]
	v_pk_mul_f32 v[14:15], v[14:15], v[136:137] op_sel_hi:[1,0]
	v_pk_mul_f32 v[20:21], v[20:21], v[136:137] op_sel_hi:[1,0]
	v_pk_mul_f32 v[22:23], v[22:23], v[136:137] op_sel_hi:[1,0]
	s_waitcnt lgkmcnt(0)
	v_mov_b32_e32 v136, v141
	v_mov_b32_e32 v137, v142
	v_mov_b32_e32 v141, v143
	v_pk_add_f32 v[136:137], v[136:137], v[140:141]
	v_pk_mul_f32 v[14:15], v[134:135], v[14:15]
	v_add_f32_e32 v136, v136, v137
	v_fmamk_f32 v136, v136, 0x3c000000, v205
	v_pk_mul_f32 v[12:13], v[132:133], v[12:13]
	v_pk_mul_f32 v[22:23], v[130:131], v[22:23]
	v_pk_mul_f32 v[20:21], v[128:129], v[20:21]
	v_rsq_f32_e32 v136, v136
	s_nop 0
	v_add_u32_e32 v140, s69, v199
	v_pk_mul_f32 v[60:61], v[60:61], v[136:137] op_sel_hi:[1,0]
	v_pk_mul_f32 v[62:63], v[62:63], v[136:137] op_sel_hi:[1,0]
	v_pk_mul_f32 v[76:77], v[76:77], v[136:137] op_sel_hi:[1,0]
	v_pk_mul_f32 v[78:79], v[78:79], v[136:137] op_sel_hi:[1,0]
	ds_read_b128 v[136:139], v140
	ds_read_b128 v[140:143], v140 offset:16
	v_pk_mul_f32 v[62:63], v[134:135], v[62:63]
	v_pk_mul_f32 v[60:61], v[132:133], v[60:61]
	v_pk_mul_f32 v[78:79], v[130:131], v[78:79]
	s_waitcnt lgkmcnt(1)
	v_mov_b32_e32 v174, v137
	v_mov_b32_e32 v175, v138
	v_mov_b32_e32 v137, v139
	v_pk_add_f32 v[136:137], v[174:175], v[136:137]
	v_pk_mul_f32 v[76:77], v[128:129], v[76:77]
	v_add_f32_e32 v136, v136, v137
	v_fmamk_f32 v136, v136, 0x3c000000, v205
	v_rsq_f32_e32 v136, v136
	s_nop 0
	v_pk_mul_f32 v[0:1], v[0:1], v[136:137] op_sel_hi:[1,0]
	v_pk_mul_f32 v[2:3], v[2:3], v[136:137] op_sel_hi:[1,0]
	v_pk_mul_f32 v[4:5], v[4:5], v[136:137] op_sel_hi:[1,0]
	v_pk_mul_f32 v[6:7], v[6:7], v[136:137] op_sel_hi:[1,0]
	s_waitcnt lgkmcnt(0)
	v_mov_b32_e32 v136, v141
	v_mov_b32_e32 v137, v142
	v_mov_b32_e32 v141, v143
	v_pk_add_f32 v[136:137], v[136:137], v[140:141]
	v_pk_mul_f32 v[2:3], v[134:135], v[2:3]
	v_add_f32_e32 v136, v136, v137
	v_fmamk_f32 v136, v136, 0x3c000000, v205
	v_pk_mul_f32 v[0:1], v[132:133], v[0:1]
	v_pk_mul_f32 v[6:7], v[130:131], v[6:7]
	v_pk_mul_f32 v[4:5], v[128:129], v[4:5]
	s_cselect_b64 s[14:15], -1, 0
	s_or_b64 s[14:15], s[26:27], s[14:15]
	v_rsq_f32_e32 v136, v136
	s_nop 0
	v_pk_mul_f32 v[24:25], v[24:25], v[136:137] op_sel_hi:[1,0]
	v_pk_mul_f32 v[26:27], v[26:27], v[136:137] op_sel_hi:[1,0]
	v_pk_mul_f32 v[44:45], v[44:45], v[136:137] op_sel_hi:[1,0]
	v_pk_mul_f32 v[46:47], v[46:47], v[136:137] op_sel_hi:[1,0]
	v_pk_mul_f32 v[26:27], v[134:135], v[26:27]
	v_pk_mul_f32 v[24:25], v[132:133], v[24:25]
	v_pk_mul_f32 v[46:47], v[130:131], v[46:47]
	v_pk_mul_f32 v[44:45], v[128:129], v[44:45]
	s_and_b64 vcc, exec, s[14:15]
	s_cbranch_vccnz .LBB0_372
;     __device__ __forceinline__ void operator()(Acc& acc, const Unit& u, int wr, int wc, int fr, int fq, LAS unsigned char* le, int wid, int lane, int& cpm) const {
;     ...
;             if (type >= 3 && wc == 0) {
; #pragma unroll
;                 for (int ai = 0; ai < 2; ++ai)
; #pragma unroll
;                     for (int m = 0; m < 4; ++m) {
;                         const int pos = (row0 + ai * 128 + wr * 64 + m * 16 + fr) & (SEQ - 1);
;                         const float* cp = rope + (size_t)pos * 16 + (fq & 1) * 8;
;                         const f32x4 c0 = *(const f32x4*)cp, c1 = *(const f32x4*)(cp + 4), s0 = *(const f32x4*)(cp + SEQ * 16), s1 = *(const f32x4*)(cp + SEQ * 16 + 4);
; #pragma unroll
;                         for (int bj = 0; bj < 2; ++bj) {
;                             f32x4 a = acc[ai][bj][m][0], b = acc[ai][bj][m][1], oa, ob;
; #pragma unroll
;                             for (int j = 0; j < 4; ++j) { oa[j] = __shfl_xor(a[j], 32); ob[j] = __shfl_xor(b[j], 32); }
;                             if (fq < 2) { a = a * c0 - oa * s0; b = b * c1 - ob * s1; } else { a = a * c0 + oa * s0; b = b * c1 + ob * s1; }
;                             acc[ai][bj][m][0] = a; acc[ai][bj][m][1] = b;
;                         }
;                     }
;             }
	v_readlane_b32 s14, v254, 16
	s_add_i32 s16, s52, s14
	s_and_b32 s14, s16, 0xfc0
	v_or_b32_e32 v128, s14, v192
	v_lshlrev_b32_e32 v156, 6, v128
	v_lshl_add_u64 v[174:175], v[166:167], 0, v[156:157]
	v_add_co_u32_e32 v132, vcc, 0x40000, v174
	global_load_dwordx4 v[128:131], v[174:175], off offset:16
	global_load_dwordx4 v[140:143], v[174:175], off
	v_addc_co_u32_e32 v133, vcc, 0, v175, vcc
	global_load_dwordx4 v[136:139], v[132:133], off
	v_lshl_add_u64 v[132:133], v[174:175], 0, s[28:29]
	global_load_dwordx4 v[132:135], v[132:133], off offset:16
	v_add_co_u32_e32 v214, vcc, 0x40000, v174
	global_load_dwordx4 v[210:213], v[174:175], off offset:1040
	global_load_dwordx4 v[222:225], v[174:175], off offset:1024
	v_addc_co_u32_e32 v215, vcc, 0, v175, vcc
	global_load_dwordx4 v[218:221], v[214:215], off offset:1024
	v_lshl_add_u64 v[214:215], v[174:175], 0, s[30:31]
	global_load_dwordx4 v[214:217], v[214:215], off offset:16
	v_add_co_u32_e32 v230, vcc, 0x40000, v174
	global_load_dwordx4 v[226:229], v[174:175], off offset:2064
	global_load_dwordx4 v[238:241], v[174:175], off offset:2048
	v_addc_co_u32_e32 v231, vcc, 0, v175, vcc
	global_load_dwordx4 v[234:237], v[230:231], off offset:2048
	v_lshl_add_u64 v[230:231], v[174:175], 0, s[34:35]
	global_load_dwordx4 v[230:233], v[230:231], off offset:16
	ds_bpermute_b32 v184, v198, v80
	ds_bpermute_b32 v186, v198, v92
	ds_bpermute_b32 v185, v198, v81
	ds_bpermute_b32 v187, v198, v93
	ds_bpermute_b32 v190, v198, v82
	ds_bpermute_b32 v208, v198, v94
	ds_bpermute_b32 v191, v198, v83
	ds_bpermute_b32 v209, v198, v95
	s_waitcnt vmcnt(11)
	v_pk_mul_f32 v[180:181], v[94:95], v[130:131]
	s_waitcnt vmcnt(10)
	v_pk_mul_f32 v[176:177], v[82:83], v[142:143]
	v_pk_mul_f32 v[178:179], v[80:81], v[140:141]
	v_pk_mul_f32 v[182:183], v[92:93], v[128:129]
	s_waitcnt vmcnt(9) lgkmcnt(5)
	v_pk_mul_f32 v[188:189], v[136:137], v[184:185]
	s_waitcnt lgkmcnt(1)
	v_pk_mul_f32 v[190:191], v[138:139], v[190:191]
	s_waitcnt vmcnt(8) lgkmcnt(0)
	v_pk_mul_f32 v[184:185], v[134:135], v[208:209]
	v_pk_mul_f32 v[186:187], v[132:133], v[186:187]
	s_and_saveexec_b64 s[14:15], s[10:11]
	s_xor_b64 s[14:15], exec, s[14:15]
	v_pk_add_f32 v[82:83], v[176:177], v[190:191]
	v_pk_add_f32 v[80:81], v[178:179], v[188:189]
	v_pk_add_f32 v[94:95], v[180:181], v[184:185]
	v_pk_add_f32 v[92:93], v[182:183], v[186:187]
	s_andn2_saveexec_b64 s[14:15], s[14:15]
	v_sub_f32_e32 v83, v177, v191
	v_sub_f32_e32 v82, v176, v190
	v_sub_f32_e32 v81, v179, v189
	v_sub_f32_e32 v80, v178, v188
	v_sub_f32_e32 v95, v181, v185
	v_sub_f32_e32 v94, v180, v184
	v_sub_f32_e32 v93, v183, v187
	v_sub_f32_e32 v92, v182, v186
	s_or_b64 exec, exec, s[14:15]
	ds_bpermute_b32 v176, v198, v120
	ds_bpermute_b32 v178, v198, v124
	ds_bpermute_b32 v177, v198, v121
	ds_bpermute_b32 v179, v198, v125
	ds_bpermute_b32 v180, v198, v122
	ds_bpermute_b32 v181, v198, v123
	ds_bpermute_b32 v182, v198, v126
	ds_bpermute_b32 v183, v198, v127
	v_pk_mul_f32 v[142:143], v[122:123], v[142:143]
	v_pk_mul_f32 v[140:141], v[120:121], v[140:141]
	s_waitcnt lgkmcnt(2)
	v_pk_mul_f32 v[138:139], v[138:139], v[180:181]
	v_pk_mul_f32 v[136:137], v[136:137], v[176:177]
	v_pk_mul_f32 v[130:131], v[126:127], v[130:131]
	v_pk_mul_f32 v[128:129], v[124:125], v[128:129]
	s_waitcnt lgkmcnt(0)
	v_pk_mul_f32 v[134:135], v[134:135], v[182:183]
	v_pk_mul_f32 v[132:133], v[132:133], v[178:179]
	s_and_saveexec_b64 s[14:15], s[10:11]
	s_xor_b64 s[14:15], exec, s[14:15]
	v_pk_add_f32 v[122:123], v[142:143], v[138:139]
	v_pk_add_f32 v[120:121], v[140:141], v[136:137]
	v_pk_add_f32 v[126:127], v[130:131], v[134:135]
	v_pk_add_f32 v[124:125], v[128:129], v[132:133]
	s_andn2_saveexec_b64 s[14:15], s[14:15]
	v_sub_f32_e32 v123, v143, v139
	v_sub_f32_e32 v122, v142, v138
	v_sub_f32_e32 v121, v141, v137
	v_sub_f32_e32 v120, v140, v136
	v_sub_f32_e32 v127, v131, v135
	v_sub_f32_e32 v126, v130, v134
	v_sub_f32_e32 v125, v129, v133
	v_sub_f32_e32 v124, v128, v132
	s_or_b64 exec, exec, s[14:15]
	v_add_co_u32_e32 v132, vcc, 0x40000, v174
	global_load_dwordx4 v[128:131], v[174:175], off offset:3088
	global_load_dwordx4 v[140:143], v[174:175], off offset:3072
	v_addc_co_u32_e32 v133, vcc, 0, v175, vcc
	global_load_dwordx4 v[136:139], v[132:133], off offset:3072
	v_lshl_add_u64 v[132:133], v[174:175], 0, s[36:37]
	global_load_dwordx4 v[132:135], v[132:133], off offset:16
	ds_bpermute_b32 v184, v198, v52
	ds_bpermute_b32 v186, v198, v68
	ds_bpermute_b32 v185, v198, v53
	ds_bpermute_b32 v187, v198, v69
	ds_bpermute_b32 v190, v198, v54
	ds_bpermute_b32 v208, v198, v70
	ds_bpermute_b32 v191, v198, v55
	ds_bpermute_b32 v209, v198, v71
	s_waitcnt vmcnt(11)
	v_pk_mul_f32 v[180:181], v[70:71], v[212:213]
	s_waitcnt vmcnt(10)
	v_pk_mul_f32 v[176:177], v[54:55], v[224:225]
	v_pk_mul_f32 v[178:179], v[52:53], v[222:223]
	v_pk_mul_f32 v[182:183], v[68:69], v[210:211]
	s_waitcnt vmcnt(9) lgkmcnt(5)
	v_pk_mul_f32 v[188:189], v[218:219], v[184:185]
	s_waitcnt lgkmcnt(1)
	v_pk_mul_f32 v[190:191], v[220:221], v[190:191]
	s_waitcnt vmcnt(8) lgkmcnt(0)
	v_pk_mul_f32 v[184:185], v[216:217], v[208:209]
	v_pk_mul_f32 v[186:187], v[214:215], v[186:187]
	s_and_saveexec_b64 s[14:15], s[10:11]
	s_xor_b64 s[14:15], exec, s[14:15]
	v_pk_add_f32 v[54:55], v[176:177], v[190:191]
	v_pk_add_f32 v[52:53], v[178:179], v[188:189]
	v_pk_add_f32 v[70:71], v[180:181], v[184:185]
	v_pk_add_f32 v[68:69], v[182:183], v[186:187]
	s_andn2_saveexec_b64 s[14:15], s[14:15]
	v_sub_f32_e32 v55, v177, v191
	v_sub_f32_e32 v54, v176, v190
	v_sub_f32_e32 v53, v179, v189
	v_sub_f32_e32 v52, v178, v188
	v_sub_f32_e32 v71, v181, v185
	v_sub_f32_e32 v70, v180, v184
	v_sub_f32_e32 v69, v183, v187
	v_sub_f32_e32 v68, v182, v186
	s_or_b64 exec, exec, s[14:15]
	ds_bpermute_b32 v176, v198, v104
	ds_bpermute_b32 v178, v198, v112
	ds_bpermute_b32 v177, v198, v105
	ds_bpermute_b32 v179, v198, v113
	ds_bpermute_b32 v180, v198, v106
	ds_bpermute_b32 v181, v198, v107
	ds_bpermute_b32 v182, v198, v114
	ds_bpermute_b32 v183, v198, v115
	v_pk_mul_f32 v[224:225], v[106:107], v[224:225]
	v_pk_mul_f32 v[222:223], v[104:105], v[222:223]
	s_waitcnt lgkmcnt(2)
;     __device__ __forceinline__ void operator()(Acc& acc, const Unit& u, int wr, int wc, int fr, int fq, LAS unsigned char* le, int wid, int lane, int& cpm) const {
;     ...
;             if (type >= 3 && wc == 0) {
; #pragma unroll
;                 for (int ai = 0; ai < 2; ++ai)
; #pragma unroll
;                     for (int m = 0; m < 4; ++m) {
;                         const int pos = (row0 + ai * 128 + wr * 64 + m * 16 + fr) & (SEQ - 1);
;                         const float* cp = rope + (size_t)pos * 16 + (fq & 1) * 8;
;                         const f32x4 c0 = *(const f32x4*)cp, c1 = *(const f32x4*)(cp + 4), s0 = *(const f32x4*)(cp + SEQ * 16), s1 = *(const f32x4*)(cp + SEQ * 16 + 4);
; #pragma unroll
;                         for (int bj = 0; bj < 2; ++bj) {
;                             f32x4 a = acc[ai][bj][m][0], b = acc[ai][bj][m][1], oa, ob;
; #pragma unroll
;                             for (int j = 0; j < 4; ++j) { oa[j] = __shfl_xor(a[j], 32); ob[j] = __shfl_xor(b[j], 32); }
;                             if (fq < 2) { a = a * c0 - oa * s0; b = b * c1 - ob * s1; } else { a = a * c0 + oa * s0; b = b * c1 + ob * s1; }
;                             acc[ai][bj][m][0] = a; acc[ai][bj][m][1] = b;
;                         }
;                     }
;             }
	v_pk_mul_f32 v[220:221], v[220:221], v[180:181]
	v_pk_mul_f32 v[218:219], v[218:219], v[176:177]
	v_pk_mul_f32 v[212:213], v[114:115], v[212:213]
	v_pk_mul_f32 v[210:211], v[112:113], v[210:211]
	s_waitcnt lgkmcnt(0)
	v_pk_mul_f32 v[216:217], v[216:217], v[182:183]
	v_pk_mul_f32 v[214:215], v[214:215], v[178:179]
	s_and_saveexec_b64 s[14:15], s[10:11]
	s_xor_b64 s[14:15], exec, s[14:15]
	v_pk_add_f32 v[106:107], v[224:225], v[220:221]
	v_pk_add_f32 v[104:105], v[222:223], v[218:219]
	v_pk_add_f32 v[114:115], v[212:213], v[216:217]
	v_pk_add_f32 v[112:113], v[210:211], v[214:215]
	s_andn2_saveexec_b64 s[14:15], s[14:15]
	v_sub_f32_e32 v107, v225, v221
	v_sub_f32_e32 v106, v224, v220
	v_sub_f32_e32 v105, v223, v219
	v_sub_f32_e32 v104, v222, v218
	v_sub_f32_e32 v115, v213, v217
	v_sub_f32_e32 v114, v212, v216
	v_sub_f32_e32 v113, v211, v215
	v_sub_f32_e32 v112, v210, v214
	s_or_b64 exec, exec, s[14:15]
	ds_bpermute_b32 v184, v198, v28
	ds_bpermute_b32 v186, v198, v36
	ds_bpermute_b32 v185, v198, v29
	ds_bpermute_b32 v187, v198, v37
	ds_bpermute_b32 v190, v198, v30
	ds_bpermute_b32 v208, v198, v38
	ds_bpermute_b32 v191, v198, v31
	ds_bpermute_b32 v209, v198, v39
	s_waitcnt vmcnt(7)
	v_pk_mul_f32 v[180:181], v[38:39], v[228:229]
	s_waitcnt vmcnt(6)
	v_pk_mul_f32 v[176:177], v[30:31], v[240:241]
	v_pk_mul_f32 v[178:179], v[28:29], v[238:239]
	v_pk_mul_f32 v[182:183], v[36:37], v[226:227]
	s_waitcnt vmcnt(5) lgkmcnt(5)
	v_pk_mul_f32 v[188:189], v[234:235], v[184:185]
	s_waitcnt lgkmcnt(1)
	v_pk_mul_f32 v[190:191], v[236:237], v[190:191]
	s_waitcnt vmcnt(4) lgkmcnt(0)
	v_pk_mul_f32 v[184:185], v[232:233], v[208:209]
	v_pk_mul_f32 v[186:187], v[230:231], v[186:187]
	s_and_saveexec_b64 s[14:15], s[10:11]
	s_xor_b64 s[14:15], exec, s[14:15]
	v_pk_add_f32 v[30:31], v[176:177], v[190:191]
	v_pk_add_f32 v[28:29], v[178:179], v[188:189]
	v_pk_add_f32 v[38:39], v[180:181], v[184:185]
	v_pk_add_f32 v[36:37], v[182:183], v[186:187]
	s_andn2_saveexec_b64 s[14:15], s[14:15]
	v_sub_f32_e32 v31, v177, v191
	v_sub_f32_e32 v30, v176, v190
	v_sub_f32_e32 v29, v179, v189
	v_sub_f32_e32 v28, v178, v188
	v_sub_f32_e32 v39, v181, v185
	v_sub_f32_e32 v38, v180, v184
	v_sub_f32_e32 v37, v183, v187
	v_sub_f32_e32 v36, v182, v186
	s_or_b64 exec, exec, s[14:15]
	ds_bpermute_b32 v176, v198, v84
	ds_bpermute_b32 v178, v198, v96
	ds_bpermute_b32 v177, v198, v85
	ds_bpermute_b32 v179, v198, v97
	ds_bpermute_b32 v180, v198, v86
	ds_bpermute_b32 v181, v198, v87
	ds_bpermute_b32 v182, v198, v98
	ds_bpermute_b32 v183, v198, v99
	v_pk_mul_f32 v[240:241], v[86:87], v[240:241]
	v_pk_mul_f32 v[238:239], v[84:85], v[238:239]
	s_waitcnt lgkmcnt(2)
	v_pk_mul_f32 v[236:237], v[236:237], v[180:181]
	v_pk_mul_f32 v[234:235], v[234:235], v[176:177]
	v_pk_mul_f32 v[228:229], v[98:99], v[228:229]
	v_pk_mul_f32 v[226:227], v[96:97], v[226:227]
	s_waitcnt lgkmcnt(0)
	v_pk_mul_f32 v[232:233], v[232:233], v[182:183]
	v_pk_mul_f32 v[230:231], v[230:231], v[178:179]
	s_and_saveexec_b64 s[14:15], s[10:11]
	s_xor_b64 s[14:15], exec, s[14:15]
	v_pk_add_f32 v[86:87], v[240:241], v[236:237]
	v_pk_add_f32 v[84:85], v[238:239], v[234:235]
	v_pk_add_f32 v[98:99], v[228:229], v[232:233]
	v_pk_add_f32 v[96:97], v[226:227], v[230:231]
	s_andn2_saveexec_b64 s[14:15], s[14:15]
	v_sub_f32_e32 v87, v241, v237
	v_sub_f32_e32 v86, v240, v236
	v_sub_f32_e32 v85, v239, v235
	v_sub_f32_e32 v84, v238, v234
	v_sub_f32_e32 v99, v229, v233
	v_sub_f32_e32 v98, v228, v232
	v_sub_f32_e32 v97, v227, v231
	v_sub_f32_e32 v96, v226, v230
	s_or_b64 exec, exec, s[14:15]
	ds_bpermute_b32 v182, v198, v8
	ds_bpermute_b32 v184, v198, v16
	ds_bpermute_b32 v183, v198, v9
	ds_bpermute_b32 v185, v198, v17
	ds_bpermute_b32 v188, v198, v10
	ds_bpermute_b32 v190, v198, v18
	ds_bpermute_b32 v189, v198, v11
	ds_bpermute_b32 v191, v198, v19
	s_waitcnt vmcnt(3)
	v_pk_mul_f32 v[178:179], v[18:19], v[130:131]
	s_waitcnt vmcnt(2)
	v_pk_mul_f32 v[174:175], v[10:11], v[142:143]
	v_pk_mul_f32 v[176:177], v[8:9], v[140:141]
	v_pk_mul_f32 v[180:181], v[16:17], v[128:129]
	s_waitcnt vmcnt(1) lgkmcnt(5)
	v_pk_mul_f32 v[186:187], v[136:137], v[182:183]
	s_waitcnt lgkmcnt(1)
	v_pk_mul_f32 v[188:189], v[138:139], v[188:189]
	s_waitcnt vmcnt(0) lgkmcnt(0)
	v_pk_mul_f32 v[182:183], v[134:135], v[190:191]
	v_pk_mul_f32 v[184:185], v[132:133], v[184:185]
	s_and_saveexec_b64 s[14:15], s[10:11]
	s_xor_b64 s[14:15], exec, s[14:15]
	v_pk_add_f32 v[10:11], v[174:175], v[188:189]
	v_pk_add_f32 v[8:9], v[176:177], v[186:187]
	v_pk_add_f32 v[18:19], v[178:179], v[182:183]
	v_pk_add_f32 v[16:17], v[180:181], v[184:185]
	s_andn2_saveexec_b64 s[14:15], s[14:15]
	v_sub_f32_e32 v11, v175, v189
	v_sub_f32_e32 v10, v174, v188
	v_sub_f32_e32 v9, v177, v187
	v_sub_f32_e32 v8, v176, v186
	v_sub_f32_e32 v19, v179, v183
	v_sub_f32_e32 v18, v178, v182
	v_sub_f32_e32 v17, v181, v185
	v_sub_f32_e32 v16, v180, v184
	s_or_b64 exec, exec, s[14:15]
	ds_bpermute_b32 v174, v198, v48
	ds_bpermute_b32 v176, v198, v64
	ds_bpermute_b32 v175, v198, v49
	ds_bpermute_b32 v177, v198, v65
	ds_bpermute_b32 v178, v198, v50
	ds_bpermute_b32 v179, v198, v51
	ds_bpermute_b32 v180, v198, v66
	ds_bpermute_b32 v181, v198, v67
	v_pk_mul_f32 v[142:143], v[50:51], v[142:143]
	v_pk_mul_f32 v[140:141], v[48:49], v[140:141]
	s_waitcnt lgkmcnt(2)
	v_pk_mul_f32 v[138:139], v[138:139], v[178:179]
	v_pk_mul_f32 v[136:137], v[136:137], v[174:175]
	v_pk_mul_f32 v[130:131], v[66:67], v[130:131]
	v_pk_mul_f32 v[128:129], v[64:65], v[128:129]
	s_waitcnt lgkmcnt(0)
;     __device__ __forceinline__ void operator()(Acc& acc, const Unit& u, int wr, int wc, int fr, int fq, LAS unsigned char* le, int wid, int lane, int& cpm) const {
;     ...
;             if (type >= 3 && wc == 0) {
; #pragma unroll
;                 for (int ai = 0; ai < 2; ++ai)
; #pragma unroll
;                     for (int m = 0; m < 4; ++m) {
;                         const int pos = (row0 + ai * 128 + wr * 64 + m * 16 + fr) & (SEQ - 1);
;                         const float* cp = rope + (size_t)pos * 16 + (fq & 1) * 8;
;                         const f32x4 c0 = *(const f32x4*)cp, c1 = *(const f32x4*)(cp + 4), s0 = *(const f32x4*)(cp + SEQ * 16), s1 = *(const f32x4*)(cp + SEQ * 16 + 4);
; #pragma unroll
;                         for (int bj = 0; bj < 2; ++bj) {
;                             f32x4 a = acc[ai][bj][m][0], b = acc[ai][bj][m][1], oa, ob;
; #pragma unroll
;                             for (int j = 0; j < 4; ++j) { oa[j] = __shfl_xor(a[j], 32); ob[j] = __shfl_xor(b[j], 32); }
;                             if (fq < 2) { a = a * c0 - oa * s0; b = b * c1 - ob * s1; } else { a = a * c0 + oa * s0; b = b * c1 + ob * s1; }
;                             acc[ai][bj][m][0] = a; acc[ai][bj][m][1] = b;
;                         }
;                     }
;             }
	v_pk_mul_f32 v[134:135], v[134:135], v[180:181]
	v_pk_mul_f32 v[132:133], v[132:133], v[176:177]
	s_and_saveexec_b64 s[14:15], s[10:11]
	s_xor_b64 s[14:15], exec, s[14:15]
	v_pk_add_f32 v[50:51], v[142:143], v[138:139]
	v_pk_add_f32 v[48:49], v[140:141], v[136:137]
	v_pk_add_f32 v[66:67], v[130:131], v[134:135]
	v_pk_add_f32 v[64:65], v[128:129], v[132:133]
	s_andn2_saveexec_b64 s[14:15], s[14:15]
	v_sub_f32_e32 v51, v143, v139
	v_sub_f32_e32 v50, v142, v138
	v_sub_f32_e32 v49, v141, v137
	v_sub_f32_e32 v48, v140, v136
	v_sub_f32_e32 v67, v131, v135
	v_sub_f32_e32 v66, v130, v134
	v_sub_f32_e32 v65, v129, v133
	v_sub_f32_e32 v64, v128, v132
	s_or_b64 exec, exec, s[14:15]
	s_addk_i32 s16, 0x80
	s_and_b32 s14, s16, 0xfc0
	v_or_b32_e32 v128, s14, v192
	v_lshlrev_b32_e32 v156, 6, v128
	v_lshl_add_u64 v[174:175], v[166:167], 0, v[156:157]
	v_add_co_u32_e32 v214, vcc, 0x40000, v174
	global_load_dwordx4 v[210:213], v[174:175], off offset:16
	global_load_dwordx4 v[222:225], v[174:175], off
	v_addc_co_u32_e32 v215, vcc, 0, v175, vcc
	global_load_dwordx4 v[218:221], v[214:215], off
	v_lshl_add_u64 v[214:215], v[174:175], 0, s[28:29]
	global_load_dwordx4 v[214:217], v[214:215], off offset:16
	v_add_co_u32_e32 v230, vcc, 0x40000, v174
	global_load_dwordx4 v[226:229], v[174:175], off offset:1040
	global_load_dwordx4 v[238:241], v[174:175], off offset:1024
	v_addc_co_u32_e32 v231, vcc, 0, v175, vcc
	global_load_dwordx4 v[234:237], v[230:231], off offset:1024
	v_lshl_add_u64 v[230:231], v[174:175], 0, s[30:31]
	global_load_dwordx4 v[230:233], v[230:231], off offset:16
	v_add_co_u32_e32 v132, vcc, 0x40000, v174
	global_load_dwordx4 v[128:131], v[174:175], off offset:2064
	global_load_dwordx4 v[140:143], v[174:175], off offset:2048
	v_addc_co_u32_e32 v133, vcc, 0, v175, vcc
	global_load_dwordx4 v[136:139], v[132:133], off offset:2048
	v_lshl_add_u64 v[132:133], v[174:175], 0, s[34:35]
	global_load_dwordx4 v[132:135], v[132:133], off offset:16
	ds_bpermute_b32 v184, v198, v56
	ds_bpermute_b32 v186, v198, v72
	ds_bpermute_b32 v185, v198, v57
	ds_bpermute_b32 v187, v198, v73
	ds_bpermute_b32 v190, v198, v58
	ds_bpermute_b32 v208, v198, v74
	ds_bpermute_b32 v191, v198, v59
	ds_bpermute_b32 v209, v198, v75
	s_waitcnt vmcnt(11)
	v_pk_mul_f32 v[180:181], v[74:75], v[212:213]
	s_waitcnt vmcnt(10)
	v_pk_mul_f32 v[176:177], v[58:59], v[224:225]
	v_pk_mul_f32 v[178:179], v[56:57], v[222:223]
	v_pk_mul_f32 v[182:183], v[72:73], v[210:211]
	s_waitcnt vmcnt(9) lgkmcnt(5)
	v_pk_mul_f32 v[188:189], v[218:219], v[184:185]
	s_waitcnt lgkmcnt(1)
	v_pk_mul_f32 v[190:191], v[220:221], v[190:191]
	s_waitcnt vmcnt(8) lgkmcnt(0)
	v_pk_mul_f32 v[184:185], v[216:217], v[208:209]
	v_pk_mul_f32 v[186:187], v[214:215], v[186:187]
	s_and_saveexec_b64 s[14:15], s[10:11]
	s_xor_b64 s[14:15], exec, s[14:15]
	v_pk_add_f32 v[58:59], v[176:177], v[190:191]
	v_pk_add_f32 v[56:57], v[178:179], v[188:189]
	v_pk_add_f32 v[74:75], v[180:181], v[184:185]
	v_pk_add_f32 v[72:73], v[182:183], v[186:187]
	s_andn2_saveexec_b64 s[14:15], s[14:15]
	v_sub_f32_e32 v59, v177, v191
	v_sub_f32_e32 v58, v176, v190
	v_sub_f32_e32 v57, v179, v189
	v_sub_f32_e32 v56, v178, v188
	v_sub_f32_e32 v75, v181, v185
	v_sub_f32_e32 v74, v180, v184
	v_sub_f32_e32 v73, v183, v187
	v_sub_f32_e32 v72, v182, v186
	s_or_b64 exec, exec, s[14:15]
	ds_bpermute_b32 v176, v198, v108
	ds_bpermute_b32 v178, v198, v116
	ds_bpermute_b32 v177, v198, v109
	ds_bpermute_b32 v179, v198, v117
	ds_bpermute_b32 v180, v198, v110
	ds_bpermute_b32 v181, v198, v111
	ds_bpermute_b32 v182, v198, v118
	ds_bpermute_b32 v183, v198, v119
	v_pk_mul_f32 v[224:225], v[110:111], v[224:225]
	v_pk_mul_f32 v[222:223], v[108:109], v[222:223]
	s_waitcnt lgkmcnt(2)
	v_pk_mul_f32 v[220:221], v[220:221], v[180:181]
	v_pk_mul_f32 v[218:219], v[218:219], v[176:177]
	v_pk_mul_f32 v[212:213], v[118:119], v[212:213]
	v_pk_mul_f32 v[210:211], v[116:117], v[210:211]
	s_waitcnt lgkmcnt(0)
	v_pk_mul_f32 v[216:217], v[216:217], v[182:183]
	v_pk_mul_f32 v[214:215], v[214:215], v[178:179]
	s_and_saveexec_b64 s[14:15], s[10:11]
	s_xor_b64 s[14:15], exec, s[14:15]
	v_pk_add_f32 v[110:111], v[224:225], v[220:221]
	v_pk_add_f32 v[108:109], v[222:223], v[218:219]
	v_pk_add_f32 v[118:119], v[212:213], v[216:217]
	v_pk_add_f32 v[116:117], v[210:211], v[214:215]
	s_andn2_saveexec_b64 s[14:15], s[14:15]
	v_sub_f32_e32 v111, v225, v221
	v_sub_f32_e32 v110, v224, v220
	v_sub_f32_e32 v109, v223, v219
	v_sub_f32_e32 v108, v222, v218
	v_sub_f32_e32 v119, v213, v217
	v_sub_f32_e32 v118, v212, v216
	v_sub_f32_e32 v117, v211, v215
	v_sub_f32_e32 v116, v210, v214
	s_or_b64 exec, exec, s[14:15]
	v_add_co_u32_e32 v214, vcc, 0x40000, v174
	global_load_dwordx4 v[210:213], v[174:175], off offset:3088
	global_load_dwordx4 v[222:225], v[174:175], off offset:3072
	v_addc_co_u32_e32 v215, vcc, 0, v175, vcc
	global_load_dwordx4 v[218:221], v[214:215], off offset:3072
	v_lshl_add_u64 v[214:215], v[174:175], 0, s[36:37]
	global_load_dwordx4 v[214:217], v[214:215], off offset:16
	ds_bpermute_b32 v184, v198, v32
	ds_bpermute_b32 v186, v198, v40
	ds_bpermute_b32 v185, v198, v33
	ds_bpermute_b32 v187, v198, v41
	ds_bpermute_b32 v190, v198, v34
	ds_bpermute_b32 v208, v198, v42
	ds_bpermute_b32 v191, v198, v35
	ds_bpermute_b32 v209, v198, v43
	s_waitcnt vmcnt(11)
	v_pk_mul_f32 v[180:181], v[42:43], v[228:229]
	s_waitcnt vmcnt(10)
	v_pk_mul_f32 v[176:177], v[34:35], v[240:241]
	v_pk_mul_f32 v[178:179], v[32:33], v[238:239]
	v_pk_mul_f32 v[182:183], v[40:41], v[226:227]
	s_waitcnt vmcnt(9) lgkmcnt(5)
	v_pk_mul_f32 v[188:189], v[234:235], v[184:185]
	s_waitcnt lgkmcnt(1)
;     __device__ __forceinline__ void operator()(Acc& acc, const Unit& u, int wr, int wc, int fr, int fq, LAS unsigned char* le, int wid, int lane, int& cpm) const {
;     ...
;             if (type >= 3 && wc == 0) {
; #pragma unroll
;                 for (int ai = 0; ai < 2; ++ai)
; #pragma unroll
;                     for (int m = 0; m < 4; ++m) {
;                         const int pos = (row0 + ai * 128 + wr * 64 + m * 16 + fr) & (SEQ - 1);
;                         const float* cp = rope + (size_t)pos * 16 + (fq & 1) * 8;
;                         const f32x4 c0 = *(const f32x4*)cp, c1 = *(const f32x4*)(cp + 4), s0 = *(const f32x4*)(cp + SEQ * 16), s1 = *(const f32x4*)(cp + SEQ * 16 + 4);
; #pragma unroll
;                         for (int bj = 0; bj < 2; ++bj) {
;                             f32x4 a = acc[ai][bj][m][0], b = acc[ai][bj][m][1], oa, ob;
; #pragma unroll
;                             for (int j = 0; j < 4; ++j) { oa[j] = __shfl_xor(a[j], 32); ob[j] = __shfl_xor(b[j], 32); }
;                             if (fq < 2) { a = a * c0 - oa * s0; b = b * c1 - ob * s1; } else { a = a * c0 + oa * s0; b = b * c1 + ob * s1; }
;                             acc[ai][bj][m][0] = a; acc[ai][bj][m][1] = b;
;                         }
;                     }
;             }
	v_pk_mul_f32 v[190:191], v[236:237], v[190:191]
	s_waitcnt vmcnt(8) lgkmcnt(0)
	v_pk_mul_f32 v[184:185], v[232:233], v[208:209]
	v_pk_mul_f32 v[186:187], v[230:231], v[186:187]
	s_and_saveexec_b64 s[14:15], s[10:11]
	s_xor_b64 s[14:15], exec, s[14:15]
	v_pk_add_f32 v[34:35], v[176:177], v[190:191]
	v_pk_add_f32 v[32:33], v[178:179], v[188:189]
	v_pk_add_f32 v[42:43], v[180:181], v[184:185]
	v_pk_add_f32 v[40:41], v[182:183], v[186:187]
	s_andn2_saveexec_b64 s[14:15], s[14:15]
	v_sub_f32_e32 v35, v177, v191
	v_sub_f32_e32 v34, v176, v190
	v_sub_f32_e32 v33, v179, v189
	v_sub_f32_e32 v32, v178, v188
	v_sub_f32_e32 v43, v181, v185
	v_sub_f32_e32 v42, v180, v184
	v_sub_f32_e32 v41, v183, v187
	v_sub_f32_e32 v40, v182, v186
	s_or_b64 exec, exec, s[14:15]
	ds_bpermute_b32 v176, v198, v88
	ds_bpermute_b32 v178, v198, v100
	ds_bpermute_b32 v177, v198, v89
	ds_bpermute_b32 v179, v198, v101
	ds_bpermute_b32 v180, v198, v90
	ds_bpermute_b32 v181, v198, v91
	ds_bpermute_b32 v182, v198, v102
	ds_bpermute_b32 v183, v198, v103
	v_pk_mul_f32 v[240:241], v[90:91], v[240:241]
	v_pk_mul_f32 v[238:239], v[88:89], v[238:239]
	s_waitcnt lgkmcnt(2)
	v_pk_mul_f32 v[236:237], v[236:237], v[180:181]
	v_pk_mul_f32 v[234:235], v[234:235], v[176:177]
	v_pk_mul_f32 v[228:229], v[102:103], v[228:229]
	v_pk_mul_f32 v[226:227], v[100:101], v[226:227]
	s_waitcnt lgkmcnt(0)
	v_pk_mul_f32 v[232:233], v[232:233], v[182:183]
	v_pk_mul_f32 v[230:231], v[230:231], v[178:179]
	s_and_saveexec_b64 s[14:15], s[10:11]
	s_xor_b64 s[14:15], exec, s[14:15]
	v_pk_add_f32 v[90:91], v[240:241], v[236:237]
	v_pk_add_f32 v[88:89], v[238:239], v[234:235]
	v_pk_add_f32 v[102:103], v[228:229], v[232:233]
	v_pk_add_f32 v[100:101], v[226:227], v[230:231]
	s_andn2_saveexec_b64 s[14:15], s[14:15]
	v_sub_f32_e32 v91, v241, v237
	v_sub_f32_e32 v90, v240, v236
	v_sub_f32_e32 v89, v239, v235
	v_sub_f32_e32 v88, v238, v234
	v_sub_f32_e32 v103, v229, v233
	v_sub_f32_e32 v102, v228, v232
	v_sub_f32_e32 v101, v227, v231
	v_sub_f32_e32 v100, v226, v230
	s_or_b64 exec, exec, s[14:15]
	ds_bpermute_b32 v184, v198, v12
	ds_bpermute_b32 v186, v198, v20
	ds_bpermute_b32 v185, v198, v13
	ds_bpermute_b32 v187, v198, v21
	ds_bpermute_b32 v190, v198, v14
	ds_bpermute_b32 v208, v198, v22
	ds_bpermute_b32 v191, v198, v15
	ds_bpermute_b32 v209, v198, v23
	s_waitcnt vmcnt(7)
	v_pk_mul_f32 v[180:181], v[22:23], v[130:131]
	s_waitcnt vmcnt(6)
	v_pk_mul_f32 v[176:177], v[14:15], v[142:143]
	v_pk_mul_f32 v[178:179], v[12:13], v[140:141]
	v_pk_mul_f32 v[182:183], v[20:21], v[128:129]
	s_waitcnt vmcnt(5) lgkmcnt(5)
	v_pk_mul_f32 v[188:189], v[136:137], v[184:185]
	s_waitcnt lgkmcnt(1)
	v_pk_mul_f32 v[190:191], v[138:139], v[190:191]
	s_waitcnt vmcnt(4) lgkmcnt(0)
	v_pk_mul_f32 v[184:185], v[134:135], v[208:209]
	v_pk_mul_f32 v[186:187], v[132:133], v[186:187]
	s_and_saveexec_b64 s[14:15], s[10:11]
	s_xor_b64 s[14:15], exec, s[14:15]
	v_pk_add_f32 v[14:15], v[176:177], v[190:191]
	v_pk_add_f32 v[12:13], v[178:179], v[188:189]
	v_pk_add_f32 v[22:23], v[180:181], v[184:185]
	v_pk_add_f32 v[20:21], v[182:183], v[186:187]
	s_andn2_saveexec_b64 s[14:15], s[14:15]
	v_sub_f32_e32 v15, v177, v191
	v_sub_f32_e32 v14, v176, v190
	v_sub_f32_e32 v13, v179, v189
	v_sub_f32_e32 v12, v178, v188
	v_sub_f32_e32 v23, v181, v185
	v_sub_f32_e32 v22, v180, v184
	v_sub_f32_e32 v21, v183, v187
	v_sub_f32_e32 v20, v182, v186
	s_or_b64 exec, exec, s[14:15]
	ds_bpermute_b32 v176, v198, v60
	ds_bpermute_b32 v178, v198, v76
	ds_bpermute_b32 v177, v198, v61
	ds_bpermute_b32 v179, v198, v77
	ds_bpermute_b32 v180, v198, v62
	ds_bpermute_b32 v181, v198, v63
	ds_bpermute_b32 v182, v198, v78
	ds_bpermute_b32 v183, v198, v79
	v_pk_mul_f32 v[142:143], v[62:63], v[142:143]
	v_pk_mul_f32 v[140:141], v[60:61], v[140:141]
	s_waitcnt lgkmcnt(2)
;     __device__ __forceinline__ void operator()(Acc& acc, const Unit& u, int wr, int wc, int fr, int fq, LAS unsigned char* le, int wid, int lane, int& cpm) const {
;     ...
;             if (type >= 3 && wc == 0) {
; #pragma unroll
;                 for (int ai = 0; ai < 2; ++ai)
; #pragma unroll
;                     for (int m = 0; m < 4; ++m) {
;                         const int pos = (row0 + ai * 128 + wr * 64 + m * 16 + fr) & (SEQ - 1);
;                         const float* cp = rope + (size_t)pos * 16 + (fq & 1) * 8;
;                         const f32x4 c0 = *(const f32x4*)cp, c1 = *(const f32x4*)(cp + 4), s0 = *(const f32x4*)(cp + SEQ * 16), s1 = *(const f32x4*)(cp + SEQ * 16 + 4);
; #pragma unroll
;                         for (int bj = 0; bj < 2; ++bj) {
;                             f32x4 a = acc[ai][bj][m][0], b = acc[ai][bj][m][1], oa, ob;
; #pragma unroll
;                             for (int j = 0; j < 4; ++j) { oa[j] = __shfl_xor(a[j], 32); ob[j] = __shfl_xor(b[j], 32); }
;                             if (fq < 2) { a = a * c0 - oa * s0; b = b * c1 - ob * s1; } else { a = a * c0 + oa * s0; b = b * c1 + ob * s1; }
;                             acc[ai][bj][m][0] = a; acc[ai][bj][m][1] = b;
;                         }
;                     }
;             }
	v_pk_mul_f32 v[138:139], v[138:139], v[180:181]
	v_pk_mul_f32 v[136:137], v[136:137], v[176:177]
	v_pk_mul_f32 v[130:131], v[78:79], v[130:131]
	v_pk_mul_f32 v[128:129], v[76:77], v[128:129]
	s_waitcnt lgkmcnt(0)
	v_pk_mul_f32 v[134:135], v[134:135], v[182:183]
	v_pk_mul_f32 v[132:133], v[132:133], v[178:179]
	s_and_saveexec_b64 s[14:15], s[10:11]
	s_xor_b64 s[14:15], exec, s[14:15]
	v_pk_add_f32 v[62:63], v[142:143], v[138:139]
	v_pk_add_f32 v[60:61], v[140:141], v[136:137]
	v_pk_add_f32 v[78:79], v[130:131], v[134:135]
	v_pk_add_f32 v[76:77], v[128:129], v[132:133]
	s_andn2_saveexec_b64 s[14:15], s[14:15]
	v_sub_f32_e32 v63, v143, v139
	v_sub_f32_e32 v62, v142, v138
	v_sub_f32_e32 v61, v141, v137
	v_sub_f32_e32 v60, v140, v136
	v_sub_f32_e32 v79, v131, v135
	v_sub_f32_e32 v78, v130, v134
	v_sub_f32_e32 v77, v129, v133
	v_sub_f32_e32 v76, v128, v132
	s_or_b64 exec, exec, s[14:15]
	ds_bpermute_b32 v182, v198, v0
	ds_bpermute_b32 v184, v198, v4
	ds_bpermute_b32 v183, v198, v1
	ds_bpermute_b32 v185, v198, v5
	ds_bpermute_b32 v188, v198, v2
	ds_bpermute_b32 v190, v198, v6
	ds_bpermute_b32 v189, v198, v3
	ds_bpermute_b32 v191, v198, v7
	s_waitcnt vmcnt(3)
	v_pk_mul_f32 v[178:179], v[6:7], v[212:213]
	s_waitcnt vmcnt(2)
	v_pk_mul_f32 v[174:175], v[2:3], v[224:225]
	v_pk_mul_f32 v[176:177], v[0:1], v[222:223]
	v_pk_mul_f32 v[180:181], v[4:5], v[210:211]
	s_waitcnt vmcnt(1) lgkmcnt(5)
	v_pk_mul_f32 v[186:187], v[218:219], v[182:183]
	s_waitcnt lgkmcnt(1)
	v_pk_mul_f32 v[188:189], v[220:221], v[188:189]
	s_waitcnt vmcnt(0) lgkmcnt(0)
	v_pk_mul_f32 v[182:183], v[216:217], v[190:191]
	v_pk_mul_f32 v[184:185], v[214:215], v[184:185]
	s_and_saveexec_b64 s[14:15], s[10:11]
	s_xor_b64 s[14:15], exec, s[14:15]
	v_pk_add_f32 v[2:3], v[174:175], v[188:189]
	v_pk_add_f32 v[0:1], v[176:177], v[186:187]
	v_pk_add_f32 v[6:7], v[178:179], v[182:183]
	v_pk_add_f32 v[4:5], v[180:181], v[184:185]
	s_andn2_saveexec_b64 s[14:15], s[14:15]
	v_sub_f32_e32 v3, v175, v189
	v_sub_f32_e32 v2, v174, v188
	v_sub_f32_e32 v1, v177, v187
	v_sub_f32_e32 v0, v176, v186
	v_sub_f32_e32 v7, v179, v183
	v_sub_f32_e32 v6, v178, v182
	v_sub_f32_e32 v5, v181, v185
	v_sub_f32_e32 v4, v180, v184
	s_or_b64 exec, exec, s[14:15]
	ds_bpermute_b32 v174, v198, v24
	ds_bpermute_b32 v176, v198, v44
	ds_bpermute_b32 v175, v198, v25
	ds_bpermute_b32 v177, v198, v45
	ds_bpermute_b32 v178, v198, v26
	ds_bpermute_b32 v179, v198, v27
	ds_bpermute_b32 v180, v198, v46
	ds_bpermute_b32 v181, v198, v47
	v_pk_mul_f32 v[224:225], v[26:27], v[224:225]
	v_pk_mul_f32 v[222:223], v[24:25], v[222:223]
	s_waitcnt lgkmcnt(2)
	v_pk_mul_f32 v[220:221], v[220:221], v[178:179]
	v_pk_mul_f32 v[218:219], v[218:219], v[174:175]
	v_pk_mul_f32 v[212:213], v[46:47], v[212:213]
	v_pk_mul_f32 v[210:211], v[44:45], v[210:211]
	s_waitcnt lgkmcnt(0)
	v_pk_mul_f32 v[216:217], v[216:217], v[180:181]
	v_pk_mul_f32 v[214:215], v[214:215], v[176:177]
	s_and_saveexec_b64 s[14:15], s[10:11]
	s_xor_b64 s[14:15], exec, s[14:15]
	v_pk_add_f32 v[26:27], v[224:225], v[220:221]
	v_pk_add_f32 v[24:25], v[222:223], v[218:219]
	v_pk_add_f32 v[46:47], v[212:213], v[216:217]
	v_pk_add_f32 v[44:45], v[210:211], v[214:215]
	s_andn2_saveexec_b64 s[14:15], s[14:15]
	v_sub_f32_e32 v27, v225, v221
	v_sub_f32_e32 v26, v224, v220
	v_sub_f32_e32 v25, v223, v219
	v_sub_f32_e32 v24, v222, v218
	v_sub_f32_e32 v47, v213, v217
	v_sub_f32_e32 v46, v212, v216
	v_sub_f32_e32 v45, v211, v215
	v_sub_f32_e32 v44, v210, v214
	s_or_b64 exec, exec, s[14:15]
